# baseline (speedup 1.0000x reference)
.Lh_no_out:
	s_cmp_eq_u32 s17, 0
	s_cselect_b32 s4, s4, s6
	s_cselect_b32 s5, s5, s7
	s_add_u32 s24, s8, s22
	s_addc_u32 s25, s9, 0
	s_add_u32 s4, s4, s21
	s_addc_u32 s5, s5, 0
	s_add_u32 s6, s4, 0x40000
	s_addc_u32 s7, s5, 0
	s_add_u32 s8, s4, 0x80000
	s_addc_u32 s9, s5, 0
	global_load_dwordx4 v[14:17], v18, s[24:25] nt
	global_load_dwordx4 v[2:5], v18, s[4:5] nt
	global_load_dwordx4 v[6:9], v18, s[6:7] nt
	s_barrier
	global_load_dwordx4 v[10:13], v18, s[8:9] nt
	s_mul_i32 s46, s3, 0xc00
	s_add_u32 s46, s46, 0x8420
	v_lshl_add_u32 v26, v1, 2, s46
	v_and_b32_e32 v38, 15, v0
	s_mul_i32 s58, s17, 0x4200
	s_add_u32 s58, s58, 0x1e0
	v_lshl_add_u32 v38, v38, 2, s58
	v_add_u32_e32 v39, 0x1600, v38
	v_add_u32_e32 v40, 0x2c00, v38
	v_mov_b32_e32 v41, 0x41fc0000
	v_mov_b32_e32 v42, 0xbf38aa3b
	s_mov_b32 s48, 0x3f940000
	s_mov_b32 s51, 0x3fb8aa3b
	s_mov_b32 s42, 0
	s_mov_b32 s43, 0
	s_mov_b32 s44, 0x7fffffff
	s_mov_b32 s45, 0x7fffffff
	s_mov_b32 s47, 0
	s_mul_i32 s58, s3, 0x1600
	s_add_u32 s58, s58, 0x320
	v_lshl_add_u32 v44, v1, 6, s58
	v_bfe_u32 v45, v1, 2, 2
	v_lshlrev_b32_e32 v45, 4, v45
	v_xor_b32_e32 v46, 16, v45
	v_xor_b32_e32 v47, 32, v45
	v_xor_b32_e32 v48, 48, v45
	v_add_u32_e32 v45, v44, v45
	v_add_u32_e32 v46, v44, v46
	v_add_u32_e32 v47, v44, v47
	v_add_u32_e32 v48, v44, v48
	s_mul_i32 s58, s2, 0x600
	s_lshl_b32 s59, s3, 8
	s_add_u32 s58, s58, s59
	s_add_u32 s10, s10, s58
	s_addc_u32 s11, s11, 0
	v_lshlrev_b32_e32 v49, 2, v1
	s_lshl_b32 s58, s2, 2
	s_add_u32 s12, s12, s58
	s_addc_u32 s13, s13, 0
	s_setprio 3
	s_cmp_lt_u32 s3, 8
	s_cbranch_scc1 .Lh_nostagger
	s_sleep 3
